# v54 + router logits pass: the 64 router-weight loads of a token run as a rolling 16-deep register prefetch (counted vmcnt) instead of 16 load-wait groups
# speedup vs baseline: 1.0083x; 1.0032x over previous
.LBB6_1829:
	v_ashrrev_i32_e32 v13, 31, v12
	v_readlane_b32 s0, v254, 4
	v_lshlrev_b64 v[4:5], 13, v[12:13]
	v_readlane_b32 s1, v254, 5
	v_readlane_b32 s6, v254, 33
	v_readlane_b32 s7, v254, 34
	v_lshl_add_u64 v[4:5], s[0:1], 0, v[4:5]
	v_lshl_add_u64 v[8:9], v[4:5], 0, v[2:3]
	global_load_dwordx4 v[88:91], v[8:9], off
	global_load_dwordx4 v[92:95], v[8:9], off offset:1024
	global_load_dwordx4 v[96:99], v[8:9], off offset:2048
	global_load_dwordx4 v[100:103], v[8:9], off offset:3072
	v_add_co_u32_e32 v84, vcc, 0x1000, v8
	s_nop 1
	v_addc_co_u32_e32 v85, vcc, 0, v9, vcc
	global_load_dwordx4 v[104:107], v[84:85], off
	global_load_dwordx4 v[108:111], v[84:85], off offset:1024
	global_load_dwordx4 v[112:115], v[84:85], off offset:2048
	global_load_dwordx4 v[116:119], v[84:85], off offset:3072
	v_add_co_u32_e32 v86, vcc, 0x2000, v22
	s_nop 1
	v_addc_co_u32_e32 v87, vcc, 0, v23, vcc
	global_load_dwordx4 v[120:123], v[86:87], off
	global_load_dwordx4 v[124:127], v[86:87], off offset:1024
	global_load_dwordx4 v[128:131], v[86:87], off offset:2048
	global_load_dwordx4 v[132:135], v[86:87], off offset:3072
	v_add_co_u32_e32 v86, vcc, 0x1000, v86
	s_nop 1
	v_addc_co_u32_e32 v87, vcc, 0, v87, vcc
	global_load_dwordx4 v[136:139], v[86:87], off
	global_load_dwordx4 v[140:143], v[86:87], off offset:1024
	global_load_dwordx4 v[144:147], v[86:87], off offset:2048
	global_load_dwordx4 v[148:151], v[86:87], off offset:3072
	v_mov_b64_e32 v[84:85], v[14:15]
	v_add_co_u32_e32 v86, vcc, 0x2000, v14
	s_nop 1
	v_addc_co_u32_e32 v87, vcc, 0, v15, vcc
	global_load_dwordx4 v[152:155], v[84:85], off offset:32
	global_load_dwordx4 v[156:159], v[84:85], off
	global_load_dwordx4 v[160:163], v[84:85], off offset:48
	global_load_dwordx4 v[164:167], v[84:85], off offset:16
	global_load_dwordx4 v[168:171], v[84:85], off offset:112
	global_load_dwordx4 v[172:175], v[84:85], off offset:96
	global_load_dwordx4 v[176:179], v[84:85], off offset:64
	global_load_dwordx4 v[184:187], v[84:85], off offset:80
	global_load_dwordx4 v[188:191], v[86:87], off
	global_load_dwordx4 v[192:195], v[86:87], off offset:32
	global_load_dwordx4 v[196:199], v[86:87], off offset:48
	global_load_dwordx4 v[200:203], v[86:87], off offset:16
	global_load_dwordx4 v[204:207], v[86:87], off offset:64
	global_load_dwordx4 v[208:211], v[86:87], off offset:112
	global_load_dwordx4 v[216:219], v[86:87], off offset:96
	global_load_dwordx4 v[220:223], v[86:87], off offset:80
	s_waitcnt vmcnt(24)
	v_mov_b64_e32 v[4:5], v[88:89]
	v_mov_b64_e32 v[6:7], v[90:91]
	v_add_co_u32_e32 v26, vcc, s45, v8
	s_mov_b64 s[8:9], 0
	s_nop 0
	v_addc_co_u32_e32 v27, vcc, 0, v9, vcc
	v_mul_f32_e32 v10, v5, v5
	v_fmac_f32_e32 v10, v4, v4
	v_fmac_f32_e32 v10, v6, v6
	v_fmac_f32_e32 v10, v7, v7
	v_mov_b64_e32 v[4:5], v[92:93]
	v_mov_b64_e32 v[6:7], v[94:95]
	v_mul_f32_e32 v5, v5, v5
	v_fmac_f32_e32 v5, v4, v4
	v_fmac_f32_e32 v5, v6, v6
	v_fmac_f32_e32 v5, v7, v7
	v_add_f32_e32 v10, v10, v5
	v_mov_b64_e32 v[4:5], v[96:97]
	v_mov_b64_e32 v[6:7], v[98:99]
	v_mul_f32_e32 v5, v5, v5
	v_fmac_f32_e32 v5, v4, v4
	v_fmac_f32_e32 v5, v6, v6
	v_fmac_f32_e32 v5, v7, v7
	v_add_f32_e32 v10, v10, v5
	v_mov_b64_e32 v[4:5], v[100:101]
	v_mov_b64_e32 v[6:7], v[102:103]
	v_mul_f32_e32 v5, v5, v5
	v_fmac_f32_e32 v5, v4, v4
	v_fmac_f32_e32 v5, v6, v6
	v_fmac_f32_e32 v5, v7, v7
	v_add_f32_e32 v30, v10, v5
	v_mov_b64_e32 v[4:5], v[104:105]
	v_mov_b64_e32 v[6:7], v[106:107]
	v_mov_b64_e32 v[8:9], v[108:109]
	v_mov_b64_e32 v[10:11], v[110:111]
	v_mov_b32_e32 v28, v4
	v_mov_b32_e32 v29, v8
	v_mov_b32_e32 v8, v5
	v_pk_mul_f32 v[4:5], v[8:9], v[8:9]
	v_mov_b32_e32 v8, v6
	v_pk_fma_f32 v[4:5], v[28:29], v[28:29], v[4:5]
	v_mov_b32_e32 v9, v10
	v_pk_fma_f32 v[4:5], v[8:9], v[8:9], v[4:5]
	v_mov_b32_e32 v10, v7
	v_pk_fma_f32 v[4:5], v[10:11], v[10:11], v[4:5]
	s_nop 0
	v_add_f32_e32 v4, v30, v4
	v_add_f32_e32 v28, v4, v5
	v_mov_b64_e32 v[4:5], v[112:113]
	v_mov_b64_e32 v[6:7], v[114:115]
	v_mov_b64_e32 v[8:9], v[116:117]
	v_mov_b64_e32 v[10:11], v[118:119]
	v_mov_b32_e32 v26, v4
	v_mov_b32_e32 v27, v8
	v_mov_b32_e32 v8, v5
	v_pk_mul_f32 v[4:5], v[8:9], v[8:9]
	v_mov_b32_e32 v8, v6
	v_pk_fma_f32 v[4:5], v[26:27], v[26:27], v[4:5]
	v_mov_b32_e32 v9, v10
	v_pk_fma_f32 v[4:5], v[8:9], v[8:9], v[4:5]
	v_mov_b32_e32 v10, v7
	v_pk_fma_f32 v[4:5], v[10:11], v[10:11], v[4:5]
	s_nop 0
	v_add_f32_e32 v4, v28, v4
	v_add_f32_e32 v4, v4, v5
	ds_bpermute_b32 v5, v25, v4
	v_mov_b64_e32 v[28:29], v[20:21]
	s_waitcnt lgkmcnt(0)
	v_add_f32_e32 v4, v4, v5
	ds_bpermute_b32 v5, v40, v4
	s_waitcnt lgkmcnt(0)
	v_add_f32_e32 v4, v4, v5
	ds_bpermute_b32 v5, v41, v4
	s_waitcnt lgkmcnt(0)
	v_add_f32_e32 v4, v4, v5
	ds_bpermute_b32 v5, v42, v4
	s_waitcnt lgkmcnt(0)
	v_add_f32_e32 v4, v4, v5
	ds_bpermute_b32 v5, v43, v4
	s_waitcnt lgkmcnt(0)
	v_add_f32_e32 v4, v4, v5
	ds_bpermute_b32 v5, v44, v4
	s_waitcnt lgkmcnt(0)
	v_add_f32_e32 v4, v4, v5
	v_fmamk_f32 v4, v4, 0x3a000000, v212
	v_cmp_gt_f32_e32 vcc, s58, v4
	v_mul_f32_e32 v5, 0x4b800000, v4
	s_nop 0
	v_cndmask_b32_e32 v4, v4, v5, vcc
	v_rsq_f32_e32 v4, v4
	s_nop 0
	v_mul_f32_e32 v5, 0x45800000, v4
	v_cndmask_b32_e32 v26, v4, v5, vcc
	v_mov_b32_e32 v4, 0
	v_mov_b32_e32 v27, v26
	v_mov_b32_e32 v5, v4
	v_mov_b32_e32 v10, v4
	v_mov_b32_e32 v11, v4
	v_mov_b32_e32 v8, v4
	v_mov_b32_e32 v9, v4
	v_mov_b32_e32 v6, v4
	v_mov_b32_e32 v7, v4
.LBB6_1830:
	s_waitcnt vmcnt(16)
	v_add_co_u32_e32 v84, vcc, 0x4000, v14
	s_nop 1
	v_addc_co_u32_e32 v85, vcc, 0, v15, vcc
	v_add_co_u32_e32 v86, vcc, 0x2000, v84
	s_nop 1
	v_addc_co_u32_e32 v87, vcc, 0, v85, vcc
	v_lshl_add_u64 v[30:31], v[28:29], 0, v[16:17]
	v_add_co_u32_e32 v76, vcc, 0x200000, v30
	v_lshl_add_u64 v[34:35], s[6:7], 0, v[16:17]
	s_nop 0
	v_addc_co_u32_e32 v77, vcc, 0, v31, vcc
	v_add_co_u32_e32 v78, vcc, s79, v34
	v_mov_b64_e32 v[30:31], v[88:89]
	v_mov_b64_e32 v[32:33], v[90:91]
	s_nop 0
	v_addc_co_u32_e32 v79, vcc, 0, v35, vcc
	v_mov_b64_e32 v[34:35], v[120:121]
	v_mov_b64_e32 v[36:37], v[122:123]
	v_lshl_add_u64 v[38:39], v[14:15], 0, s[8:9]
	s_waitcnt vmcnt(15)
	v_mov_b64_e32 v[46:47], v[152:153]
	v_mov_b64_e32 v[48:49], v[154:155]
	global_load_dwordx4 v[152:155], v[84:85], off offset:32
	s_waitcnt vmcnt(15)
	v_mov_b64_e32 v[50:51], v[156:157]
	v_mov_b64_e32 v[52:53], v[158:159]
	global_load_dwordx4 v[156:159], v[84:85], off
	s_waitcnt vmcnt(15)
	v_mov_b64_e32 v[54:55], v[160:161]
	v_mov_b64_e32 v[56:57], v[162:163]
	global_load_dwordx4 v[160:163], v[84:85], off offset:48
	s_waitcnt vmcnt(15)
	v_mov_b64_e32 v[58:59], v[164:165]
	v_mov_b64_e32 v[60:61], v[166:167]
	global_load_dwordx4 v[164:167], v[84:85], off offset:16
	s_mov_b64 s[0:1], 0x2000
	s_add_u32 s8, s8, 0x4000
	s_addc_u32 s9, s9, 0
	s_add_u32 s6, s6, 0x800
	s_addc_u32 s7, s7, 0
	v_lshl_add_u64 v[28:29], v[28:29], 0, s[56:57]
	s_cmp_lg_u32 s8, 0x10000
	v_pk_mul_f32 v[30:31], v[26:27], v[30:31]
	v_pk_mul_f32 v[34:35], v[30:31], v[34:35]
	v_mov_b32_e32 v31, v57
	v_mul_f32_e32 v80, v34, v60
	v_mov_b32_e32 v30, v61
	s_waitcnt vmcnt(15)
	v_mov_b64_e32 v[60:61], v[168:169]
	v_mov_b64_e32 v[62:63], v[170:171]
	global_load_dwordx4 v[168:171], v[84:85], off offset:112
	s_waitcnt vmcnt(15)
	v_mov_b64_e32 v[64:65], v[172:173]
	v_mov_b64_e32 v[66:67], v[174:175]
	global_load_dwordx4 v[172:175], v[84:85], off offset:96
	s_waitcnt vmcnt(15)
	v_mov_b64_e32 v[68:69], v[176:177]
	v_mov_b64_e32 v[70:71], v[178:179]
	global_load_dwordx4 v[176:179], v[84:85], off offset:64
	s_waitcnt vmcnt(15)
	v_mov_b64_e32 v[72:73], v[184:185]
	v_mov_b64_e32 v[74:75], v[186:187]
	global_load_dwordx4 v[184:187], v[84:85], off offset:80
	v_pk_mul_f32 v[82:83], v[34:35], v[30:31]
	v_pk_fma_f32 v[10:11], v[34:35], v[50:51], v[10:11] op_sel_hi:[0,1,1]
	v_pk_mul_f32 v[30:31], v[26:27], v[32:33]
	v_pk_fma_f32 v[6:7], v[34:35], v[58:59], v[6:7] op_sel_hi:[0,1,1]
	v_pk_fma_f32 v[10:11], v[34:35], v[46:47], v[10:11] op_sel:[1,0,0]
	v_pk_mul_f32 v[46:47], v[30:31], v[36:37]
	v_pk_fma_f32 v[6:7], v[34:35], v[54:55], v[6:7] op_sel:[1,0,0]
	v_mov_b32_e32 v81, v82
	v_mul_f32_e32 v56, v35, v56
	v_pk_fma_f32 v[8:9], v[34:35], v[52:53], v[8:9] op_sel_hi:[0,1,1]
	v_pk_add_f32 v[4:5], v[4:5], v[80:81]
	v_mov_b32_e32 v57, v83
	v_pk_fma_f32 v[8:9], v[34:35], v[48:49], v[8:9] op_sel:[1,0,0]
	v_pk_add_f32 v[4:5], v[4:5], v[56:57]
	v_lshl_add_u64 v[58:59], v[38:39], 0, s[0:1]
	s_mov_b64 s[0:1], 0x2040
	v_mov_b32_e32 v31, v63
	v_pk_fma_f32 v[10:11], v[46:47], v[68:69], v[10:11] op_sel_hi:[0,1,1]
	v_mov_b32_e32 v30, v75
	v_mul_f32_e32 v50, v46, v74
	v_pk_mul_f32 v[74:75], v[46:47], v[30:31]
	v_pk_fma_f32 v[6:7], v[46:47], v[72:73], v[6:7] op_sel_hi:[0,1,1]
	v_pk_fma_f32 v[32:33], v[46:47], v[60:61], v[6:7] op_sel:[1,0,0]
	v_mul_f32_e32 v6, v47, v62
	v_mov_b32_e32 v51, v74
	v_add_co_u32_e32 v62, vcc, s79, v38
	v_pk_fma_f32 v[8:9], v[46:47], v[70:71], v[8:9] op_sel_hi:[0,1,1]
	v_pk_add_f32 v[4:5], v[4:5], v[50:51]
	v_mov_b32_e32 v7, v75
	v_addc_co_u32_e32 v63, vcc, 0, v39, vcc
	v_pk_fma_f32 v[36:37], v[46:47], v[64:65], v[10:11] op_sel:[1,0,0]
	v_pk_fma_f32 v[30:31], v[46:47], v[66:67], v[8:9] op_sel:[1,0,0]
	v_pk_add_f32 v[34:35], v[4:5], v[6:7]
	v_mov_b64_e32 v[4:5], v[92:93]
	v_mov_b64_e32 v[6:7], v[94:95]
	v_mov_b64_e32 v[8:9], v[124:125]
	v_mov_b64_e32 v[10:11], v[126:127]
	s_waitcnt vmcnt(15)
	v_mov_b64_e32 v[46:47], v[188:189]
	v_mov_b64_e32 v[48:49], v[190:191]
	global_load_dwordx4 v[188:191], v[86:87], off
	s_waitcnt vmcnt(15)
	v_mov_b64_e32 v[50:51], v[192:193]
	v_mov_b64_e32 v[52:53], v[194:195]
	global_load_dwordx4 v[192:195], v[86:87], off offset:32
	s_waitcnt vmcnt(15)
	v_mov_b64_e32 v[54:55], v[196:197]
	v_mov_b64_e32 v[56:57], v[198:199]
	global_load_dwordx4 v[196:199], v[86:87], off offset:48
	s_nop 0
	s_waitcnt vmcnt(15)
	v_mov_b64_e32 v[58:59], v[200:201]
	v_mov_b64_e32 v[60:61], v[202:203]
	global_load_dwordx4 v[200:203], v[86:87], off offset:16
	v_pk_mul_f32 v[4:5], v[26:27], v[4:5]
	v_pk_mul_f32 v[4:5], v[4:5], v[8:9]
	v_mov_b32_e32 v8, v61
	v_mov_b32_e32 v9, v57
	v_mul_f32_e32 v76, v4, v60
	v_pk_mul_f32 v[78:79], v[4:5], v[8:9]
	v_lshl_add_u64 v[8:9], v[38:39], 0, s[0:1]
	s_waitcnt vmcnt(15)
	v_mov_b64_e32 v[60:61], v[204:205]
	v_mov_b64_e32 v[62:63], v[206:207]
	global_load_dwordx4 v[204:207], v[86:87], off offset:64
	s_nop 0
	s_waitcnt vmcnt(15)
	v_mov_b64_e32 v[64:65], v[208:209]
	v_mov_b64_e32 v[66:67], v[210:211]
	global_load_dwordx4 v[208:211], v[86:87], off offset:112
	s_waitcnt vmcnt(15)
	v_mov_b64_e32 v[68:69], v[216:217]
	v_mov_b64_e32 v[70:71], v[218:219]
	global_load_dwordx4 v[216:219], v[86:87], off offset:96
	s_waitcnt vmcnt(15)
	v_mov_b64_e32 v[72:73], v[220:221]
	v_mov_b64_e32 v[74:75], v[222:223]
	global_load_dwordx4 v[220:223], v[86:87], off offset:80
	v_pk_fma_f32 v[8:9], v[4:5], v[46:47], v[36:37] op_sel_hi:[0,1,1]
	v_pk_mul_f32 v[6:7], v[26:27], v[6:7]
	v_pk_fma_f32 v[8:9], v[4:5], v[50:51], v[8:9] op_sel:[1,0,0]
	v_pk_mul_f32 v[36:37], v[6:7], v[10:11]
	v_mov_b32_e32 v77, v78
	v_mul_f32_e32 v56, v5, v56
	v_mov_b32_e32 v57, v79
	v_mov_b32_e32 v7, v67
	v_mov_b32_e32 v6, v75
	v_pk_mul_f32 v[46:47], v[36:37], v[6:7]
	v_pk_fma_f32 v[6:7], v[36:37], v[60:61], v[8:9] op_sel_hi:[0,1,1]
	v_pk_fma_f32 v[10:11], v[36:37], v[68:69], v[6:7] op_sel:[1,0,0]
	v_pk_fma_f32 v[6:7], v[4:5], v[48:49], v[30:31] op_sel_hi:[0,1,1]
	v_pk_fma_f32 v[6:7], v[4:5], v[52:53], v[6:7] op_sel:[1,0,0]
	v_pk_add_f32 v[30:31], v[34:35], v[76:77]
	v_pk_fma_f32 v[6:7], v[36:37], v[62:63], v[6:7] op_sel_hi:[0,1,1]
	v_pk_fma_f32 v[8:9], v[36:37], v[70:71], v[6:7] op_sel:[1,0,0]
	v_pk_fma_f32 v[6:7], v[4:5], v[58:59], v[32:33] op_sel_hi:[0,1,1]
	v_pk_fma_f32 v[4:5], v[4:5], v[54:55], v[6:7] op_sel:[1,0,0]
	v_mul_f32_e32 v38, v36, v74
	v_pk_fma_f32 v[4:5], v[36:37], v[72:73], v[4:5] op_sel_hi:[0,1,1]
	v_pk_add_f32 v[30:31], v[30:31], v[56:57]
	v_mov_b32_e32 v39, v46
	v_pk_fma_f32 v[6:7], v[36:37], v[64:65], v[4:5] op_sel:[1,0,0]
	v_mul_f32_e32 v4, v37, v66
	v_pk_add_f32 v[30:31], v[30:31], v[38:39]
	v_mov_b32_e32 v5, v47
	v_pk_add_f32 v[4:5], v[30:31], v[4:5]
	v_add_co_u32_e32 v84, vcc, 0x8000, v14
	s_nop 1
	v_addc_co_u32_e32 v85, vcc, 0, v15, vcc
	v_add_co_u32_e32 v86, vcc, 0x2000, v84
	s_nop 1
	v_addc_co_u32_e32 v87, vcc, 0, v85, vcc
	v_lshl_add_u64 v[30:31], v[28:29], 0, v[16:17]
	v_add_co_u32_e32 v76, vcc, 0x200000, v30
	v_lshl_add_u64 v[34:35], s[6:7], 0, v[16:17]
	s_nop 0
	v_addc_co_u32_e32 v77, vcc, 0, v31, vcc
	v_add_co_u32_e32 v78, vcc, s79, v34
	v_mov_b64_e32 v[30:31], v[96:97]
	v_mov_b64_e32 v[32:33], v[98:99]
	s_nop 0
	v_addc_co_u32_e32 v79, vcc, 0, v35, vcc
	v_mov_b64_e32 v[34:35], v[128:129]
	v_mov_b64_e32 v[36:37], v[130:131]
	v_lshl_add_u64 v[38:39], v[14:15], 0, s[8:9]
	s_waitcnt vmcnt(15)
	v_mov_b64_e32 v[46:47], v[152:153]
	v_mov_b64_e32 v[48:49], v[154:155]
	global_load_dwordx4 v[152:155], v[84:85], off offset:32
	s_waitcnt vmcnt(15)
	v_mov_b64_e32 v[50:51], v[156:157]
	v_mov_b64_e32 v[52:53], v[158:159]
	global_load_dwordx4 v[156:159], v[84:85], off
	s_waitcnt vmcnt(15)
	v_mov_b64_e32 v[54:55], v[160:161]
	v_mov_b64_e32 v[56:57], v[162:163]
	global_load_dwordx4 v[160:163], v[84:85], off offset:48
	s_waitcnt vmcnt(15)
	v_mov_b64_e32 v[58:59], v[164:165]
	v_mov_b64_e32 v[60:61], v[166:167]
	global_load_dwordx4 v[164:167], v[84:85], off offset:16
	s_mov_b64 s[0:1], 0x2000
	s_add_u32 s8, s8, 0x4000
	s_addc_u32 s9, s9, 0
	s_add_u32 s6, s6, 0x800
	s_addc_u32 s7, s7, 0
	v_lshl_add_u64 v[28:29], v[28:29], 0, s[56:57]
	s_cmp_lg_u32 s8, 0x10000
	v_pk_mul_f32 v[30:31], v[26:27], v[30:31]
	v_pk_mul_f32 v[34:35], v[30:31], v[34:35]
	v_mov_b32_e32 v31, v57
	v_mul_f32_e32 v80, v34, v60
	v_mov_b32_e32 v30, v61
	s_waitcnt vmcnt(15)
	v_mov_b64_e32 v[60:61], v[168:169]
	v_mov_b64_e32 v[62:63], v[170:171]
	global_load_dwordx4 v[168:171], v[84:85], off offset:112
	s_waitcnt vmcnt(15)
	v_mov_b64_e32 v[64:65], v[172:173]
	v_mov_b64_e32 v[66:67], v[174:175]
	global_load_dwordx4 v[172:175], v[84:85], off offset:96
	s_waitcnt vmcnt(15)
	v_mov_b64_e32 v[68:69], v[176:177]
	v_mov_b64_e32 v[70:71], v[178:179]
	global_load_dwordx4 v[176:179], v[84:85], off offset:64
	s_waitcnt vmcnt(15)
	v_mov_b64_e32 v[72:73], v[184:185]
	v_mov_b64_e32 v[74:75], v[186:187]
	global_load_dwordx4 v[184:187], v[84:85], off offset:80
	v_pk_mul_f32 v[82:83], v[34:35], v[30:31]
	v_pk_fma_f32 v[10:11], v[34:35], v[50:51], v[10:11] op_sel_hi:[0,1,1]
	v_pk_mul_f32 v[30:31], v[26:27], v[32:33]
	v_pk_fma_f32 v[6:7], v[34:35], v[58:59], v[6:7] op_sel_hi:[0,1,1]
	v_pk_fma_f32 v[10:11], v[34:35], v[46:47], v[10:11] op_sel:[1,0,0]
	v_pk_mul_f32 v[46:47], v[30:31], v[36:37]
	v_pk_fma_f32 v[6:7], v[34:35], v[54:55], v[6:7] op_sel:[1,0,0]
	v_mov_b32_e32 v81, v82
	v_mul_f32_e32 v56, v35, v56
	v_pk_fma_f32 v[8:9], v[34:35], v[52:53], v[8:9] op_sel_hi:[0,1,1]
	v_pk_add_f32 v[4:5], v[4:5], v[80:81]
	v_mov_b32_e32 v57, v83
	v_pk_fma_f32 v[8:9], v[34:35], v[48:49], v[8:9] op_sel:[1,0,0]
	v_pk_add_f32 v[4:5], v[4:5], v[56:57]
	v_lshl_add_u64 v[58:59], v[38:39], 0, s[0:1]
	s_mov_b64 s[0:1], 0x2040
	v_mov_b32_e32 v31, v63
	v_pk_fma_f32 v[10:11], v[46:47], v[68:69], v[10:11] op_sel_hi:[0,1,1]
	v_mov_b32_e32 v30, v75
	v_mul_f32_e32 v50, v46, v74
	v_pk_mul_f32 v[74:75], v[46:47], v[30:31]
	v_pk_fma_f32 v[6:7], v[46:47], v[72:73], v[6:7] op_sel_hi:[0,1,1]
	v_pk_fma_f32 v[32:33], v[46:47], v[60:61], v[6:7] op_sel:[1,0,0]
	v_mul_f32_e32 v6, v47, v62
	v_mov_b32_e32 v51, v74
	v_add_co_u32_e32 v62, vcc, s79, v38
	v_pk_fma_f32 v[8:9], v[46:47], v[70:71], v[8:9] op_sel_hi:[0,1,1]
	v_pk_add_f32 v[4:5], v[4:5], v[50:51]
	v_mov_b32_e32 v7, v75
	v_addc_co_u32_e32 v63, vcc, 0, v39, vcc
	v_pk_fma_f32 v[36:37], v[46:47], v[64:65], v[10:11] op_sel:[1,0,0]
	v_pk_fma_f32 v[30:31], v[46:47], v[66:67], v[8:9] op_sel:[1,0,0]
	v_pk_add_f32 v[34:35], v[4:5], v[6:7]
	v_mov_b64_e32 v[4:5], v[100:101]
	v_mov_b64_e32 v[6:7], v[102:103]
	v_mov_b64_e32 v[8:9], v[132:133]
	v_mov_b64_e32 v[10:11], v[134:135]
	s_waitcnt vmcnt(15)
	v_mov_b64_e32 v[46:47], v[188:189]
	v_mov_b64_e32 v[48:49], v[190:191]
	global_load_dwordx4 v[188:191], v[86:87], off
	s_waitcnt vmcnt(15)
	v_mov_b64_e32 v[50:51], v[192:193]
	v_mov_b64_e32 v[52:53], v[194:195]
	global_load_dwordx4 v[192:195], v[86:87], off offset:32
	s_waitcnt vmcnt(15)
	v_mov_b64_e32 v[54:55], v[196:197]
	v_mov_b64_e32 v[56:57], v[198:199]
	global_load_dwordx4 v[196:199], v[86:87], off offset:48
	s_nop 0
	s_waitcnt vmcnt(15)
	v_mov_b64_e32 v[58:59], v[200:201]
	v_mov_b64_e32 v[60:61], v[202:203]
	global_load_dwordx4 v[200:203], v[86:87], off offset:16
	v_pk_mul_f32 v[4:5], v[26:27], v[4:5]
	v_pk_mul_f32 v[4:5], v[4:5], v[8:9]
	v_mov_b32_e32 v8, v61
	v_mov_b32_e32 v9, v57
	v_mul_f32_e32 v76, v4, v60
	v_pk_mul_f32 v[78:79], v[4:5], v[8:9]
	v_lshl_add_u64 v[8:9], v[38:39], 0, s[0:1]
	s_waitcnt vmcnt(15)
	v_mov_b64_e32 v[60:61], v[204:205]
	v_mov_b64_e32 v[62:63], v[206:207]
	global_load_dwordx4 v[204:207], v[86:87], off offset:64
	s_nop 0
	s_waitcnt vmcnt(15)
	v_mov_b64_e32 v[64:65], v[208:209]
	v_mov_b64_e32 v[66:67], v[210:211]
	global_load_dwordx4 v[208:211], v[86:87], off offset:112
	s_waitcnt vmcnt(15)
	v_mov_b64_e32 v[68:69], v[216:217]
	v_mov_b64_e32 v[70:71], v[218:219]
	global_load_dwordx4 v[216:219], v[86:87], off offset:96
	s_waitcnt vmcnt(15)
	v_mov_b64_e32 v[72:73], v[220:221]
	v_mov_b64_e32 v[74:75], v[222:223]
	global_load_dwordx4 v[220:223], v[86:87], off offset:80
	v_pk_fma_f32 v[8:9], v[4:5], v[46:47], v[36:37] op_sel_hi:[0,1,1]
	v_pk_mul_f32 v[6:7], v[26:27], v[6:7]
	v_pk_fma_f32 v[8:9], v[4:5], v[50:51], v[8:9] op_sel:[1,0,0]
	v_pk_mul_f32 v[36:37], v[6:7], v[10:11]
	v_mov_b32_e32 v77, v78
	v_mul_f32_e32 v56, v5, v56
	v_mov_b32_e32 v57, v79
	v_mov_b32_e32 v7, v67
	v_mov_b32_e32 v6, v75
	v_pk_mul_f32 v[46:47], v[36:37], v[6:7]
	v_pk_fma_f32 v[6:7], v[36:37], v[60:61], v[8:9] op_sel_hi:[0,1,1]
	v_pk_fma_f32 v[10:11], v[36:37], v[68:69], v[6:7] op_sel:[1,0,0]
	v_pk_fma_f32 v[6:7], v[4:5], v[48:49], v[30:31] op_sel_hi:[0,1,1]
	v_pk_fma_f32 v[6:7], v[4:5], v[52:53], v[6:7] op_sel:[1,0,0]
	v_pk_add_f32 v[30:31], v[34:35], v[76:77]
	v_pk_fma_f32 v[6:7], v[36:37], v[62:63], v[6:7] op_sel_hi:[0,1,1]
	v_pk_fma_f32 v[8:9], v[36:37], v[70:71], v[6:7] op_sel:[1,0,0]
	v_pk_fma_f32 v[6:7], v[4:5], v[58:59], v[32:33] op_sel_hi:[0,1,1]
	v_pk_fma_f32 v[4:5], v[4:5], v[54:55], v[6:7] op_sel:[1,0,0]
	v_mul_f32_e32 v38, v36, v74
	v_pk_fma_f32 v[4:5], v[36:37], v[72:73], v[4:5] op_sel_hi:[0,1,1]
	v_pk_add_f32 v[30:31], v[30:31], v[56:57]
	v_mov_b32_e32 v39, v46
	v_pk_fma_f32 v[6:7], v[36:37], v[64:65], v[4:5] op_sel:[1,0,0]
	v_mul_f32_e32 v4, v37, v66
	v_pk_add_f32 v[30:31], v[30:31], v[38:39]
	v_mov_b32_e32 v5, v47
	v_pk_add_f32 v[4:5], v[30:31], v[4:5]
	v_add_co_u32_e32 v84, vcc, 0xc000, v14
	s_nop 1
	v_addc_co_u32_e32 v85, vcc, 0, v15, vcc
	v_add_co_u32_e32 v86, vcc, 0x2000, v84
	s_nop 1
	v_addc_co_u32_e32 v87, vcc, 0, v85, vcc
	v_lshl_add_u64 v[30:31], v[28:29], 0, v[16:17]
	v_add_co_u32_e32 v76, vcc, 0x200000, v30
	v_lshl_add_u64 v[34:35], s[6:7], 0, v[16:17]
	s_nop 0
	v_addc_co_u32_e32 v77, vcc, 0, v31, vcc
	v_add_co_u32_e32 v78, vcc, s79, v34
	v_mov_b64_e32 v[30:31], v[104:105]
	v_mov_b64_e32 v[32:33], v[106:107]
	s_nop 0
	v_addc_co_u32_e32 v79, vcc, 0, v35, vcc
	v_mov_b64_e32 v[34:35], v[136:137]
	v_mov_b64_e32 v[36:37], v[138:139]
	v_lshl_add_u64 v[38:39], v[14:15], 0, s[8:9]
	s_waitcnt vmcnt(15)
	v_mov_b64_e32 v[46:47], v[152:153]
	v_mov_b64_e32 v[48:49], v[154:155]
	global_load_dwordx4 v[152:155], v[84:85], off offset:32
	s_waitcnt vmcnt(15)
	v_mov_b64_e32 v[50:51], v[156:157]
	v_mov_b64_e32 v[52:53], v[158:159]
	global_load_dwordx4 v[156:159], v[84:85], off
	s_waitcnt vmcnt(15)
	v_mov_b64_e32 v[54:55], v[160:161]
	v_mov_b64_e32 v[56:57], v[162:163]
	global_load_dwordx4 v[160:163], v[84:85], off offset:48
	s_waitcnt vmcnt(15)
	v_mov_b64_e32 v[58:59], v[164:165]
	v_mov_b64_e32 v[60:61], v[166:167]
	global_load_dwordx4 v[164:167], v[84:85], off offset:16
	s_mov_b64 s[0:1], 0x2000
	s_add_u32 s8, s8, 0x4000
	s_addc_u32 s9, s9, 0
	s_add_u32 s6, s6, 0x800
	s_addc_u32 s7, s7, 0
	v_lshl_add_u64 v[28:29], v[28:29], 0, s[56:57]
	s_cmp_lg_u32 s8, 0x10000
	v_pk_mul_f32 v[30:31], v[26:27], v[30:31]
	v_pk_mul_f32 v[34:35], v[30:31], v[34:35]
	v_mov_b32_e32 v31, v57
	v_mul_f32_e32 v80, v34, v60
	v_mov_b32_e32 v30, v61
	s_waitcnt vmcnt(15)
	v_mov_b64_e32 v[60:61], v[168:169]
	v_mov_b64_e32 v[62:63], v[170:171]
	global_load_dwordx4 v[168:171], v[84:85], off offset:112
	s_waitcnt vmcnt(15)
	v_mov_b64_e32 v[64:65], v[172:173]
	v_mov_b64_e32 v[66:67], v[174:175]
	global_load_dwordx4 v[172:175], v[84:85], off offset:96
	s_waitcnt vmcnt(15)
	v_mov_b64_e32 v[68:69], v[176:177]
	v_mov_b64_e32 v[70:71], v[178:179]
	global_load_dwordx4 v[176:179], v[84:85], off offset:64
	s_waitcnt vmcnt(15)
	v_mov_b64_e32 v[72:73], v[184:185]
	v_mov_b64_e32 v[74:75], v[186:187]
	global_load_dwordx4 v[184:187], v[84:85], off offset:80
	v_pk_mul_f32 v[82:83], v[34:35], v[30:31]
	v_pk_fma_f32 v[10:11], v[34:35], v[50:51], v[10:11] op_sel_hi:[0,1,1]
	v_pk_mul_f32 v[30:31], v[26:27], v[32:33]
	v_pk_fma_f32 v[6:7], v[34:35], v[58:59], v[6:7] op_sel_hi:[0,1,1]
	v_pk_fma_f32 v[10:11], v[34:35], v[46:47], v[10:11] op_sel:[1,0,0]
	v_pk_mul_f32 v[46:47], v[30:31], v[36:37]
	v_pk_fma_f32 v[6:7], v[34:35], v[54:55], v[6:7] op_sel:[1,0,0]
	v_mov_b32_e32 v81, v82
	v_mul_f32_e32 v56, v35, v56
	v_pk_fma_f32 v[8:9], v[34:35], v[52:53], v[8:9] op_sel_hi:[0,1,1]
	v_pk_add_f32 v[4:5], v[4:5], v[80:81]
	v_mov_b32_e32 v57, v83
	v_pk_fma_f32 v[8:9], v[34:35], v[48:49], v[8:9] op_sel:[1,0,0]
	v_pk_add_f32 v[4:5], v[4:5], v[56:57]
	v_lshl_add_u64 v[58:59], v[38:39], 0, s[0:1]
	s_mov_b64 s[0:1], 0x2040
	v_mov_b32_e32 v31, v63
	v_pk_fma_f32 v[10:11], v[46:47], v[68:69], v[10:11] op_sel_hi:[0,1,1]
	v_mov_b32_e32 v30, v75
	v_mul_f32_e32 v50, v46, v74
	v_pk_mul_f32 v[74:75], v[46:47], v[30:31]
	v_pk_fma_f32 v[6:7], v[46:47], v[72:73], v[6:7] op_sel_hi:[0,1,1]
	v_pk_fma_f32 v[32:33], v[46:47], v[60:61], v[6:7] op_sel:[1,0,0]
	v_mul_f32_e32 v6, v47, v62
	v_mov_b32_e32 v51, v74
	v_add_co_u32_e32 v62, vcc, s79, v38
	v_pk_fma_f32 v[8:9], v[46:47], v[70:71], v[8:9] op_sel_hi:[0,1,1]
	v_pk_add_f32 v[4:5], v[4:5], v[50:51]
	v_mov_b32_e32 v7, v75
	v_addc_co_u32_e32 v63, vcc, 0, v39, vcc
	v_pk_fma_f32 v[36:37], v[46:47], v[64:65], v[10:11] op_sel:[1,0,0]
	v_pk_fma_f32 v[30:31], v[46:47], v[66:67], v[8:9] op_sel:[1,0,0]
	v_pk_add_f32 v[34:35], v[4:5], v[6:7]
	v_mov_b64_e32 v[4:5], v[108:109]
	v_mov_b64_e32 v[6:7], v[110:111]
	v_mov_b64_e32 v[8:9], v[140:141]
	v_mov_b64_e32 v[10:11], v[142:143]
	s_waitcnt vmcnt(15)
	v_mov_b64_e32 v[46:47], v[188:189]
	v_mov_b64_e32 v[48:49], v[190:191]
	global_load_dwordx4 v[188:191], v[86:87], off
	s_waitcnt vmcnt(15)
	v_mov_b64_e32 v[50:51], v[192:193]
	v_mov_b64_e32 v[52:53], v[194:195]
	global_load_dwordx4 v[192:195], v[86:87], off offset:32
	s_waitcnt vmcnt(15)
	v_mov_b64_e32 v[54:55], v[196:197]
	v_mov_b64_e32 v[56:57], v[198:199]
	global_load_dwordx4 v[196:199], v[86:87], off offset:48
	s_nop 0
	s_waitcnt vmcnt(15)
	v_mov_b64_e32 v[58:59], v[200:201]
	v_mov_b64_e32 v[60:61], v[202:203]
	global_load_dwordx4 v[200:203], v[86:87], off offset:16
	v_pk_mul_f32 v[4:5], v[26:27], v[4:5]
	v_pk_mul_f32 v[4:5], v[4:5], v[8:9]
	v_mov_b32_e32 v8, v61
	v_mov_b32_e32 v9, v57
	v_mul_f32_e32 v76, v4, v60
	v_pk_mul_f32 v[78:79], v[4:5], v[8:9]
	v_lshl_add_u64 v[8:9], v[38:39], 0, s[0:1]
	s_waitcnt vmcnt(15)
	v_mov_b64_e32 v[60:61], v[204:205]
	v_mov_b64_e32 v[62:63], v[206:207]
	global_load_dwordx4 v[204:207], v[86:87], off offset:64
	s_nop 0
	s_waitcnt vmcnt(15)
	v_mov_b64_e32 v[64:65], v[208:209]
	v_mov_b64_e32 v[66:67], v[210:211]
	global_load_dwordx4 v[208:211], v[86:87], off offset:112
	s_waitcnt vmcnt(15)
	v_mov_b64_e32 v[68:69], v[216:217]
	v_mov_b64_e32 v[70:71], v[218:219]
	global_load_dwordx4 v[216:219], v[86:87], off offset:96
	s_waitcnt vmcnt(15)
	v_mov_b64_e32 v[72:73], v[220:221]
	v_mov_b64_e32 v[74:75], v[222:223]
	global_load_dwordx4 v[220:223], v[86:87], off offset:80
	v_pk_fma_f32 v[8:9], v[4:5], v[46:47], v[36:37] op_sel_hi:[0,1,1]
	v_pk_mul_f32 v[6:7], v[26:27], v[6:7]
	v_pk_fma_f32 v[8:9], v[4:5], v[50:51], v[8:9] op_sel:[1,0,0]
	v_pk_mul_f32 v[36:37], v[6:7], v[10:11]
	v_mov_b32_e32 v77, v78
	v_mul_f32_e32 v56, v5, v56
	v_mov_b32_e32 v57, v79
	v_mov_b32_e32 v7, v67
	v_mov_b32_e32 v6, v75
	v_pk_mul_f32 v[46:47], v[36:37], v[6:7]
	v_pk_fma_f32 v[6:7], v[36:37], v[60:61], v[8:9] op_sel_hi:[0,1,1]
	v_pk_fma_f32 v[10:11], v[36:37], v[68:69], v[6:7] op_sel:[1,0,0]
	v_pk_fma_f32 v[6:7], v[4:5], v[48:49], v[30:31] op_sel_hi:[0,1,1]
	v_pk_fma_f32 v[6:7], v[4:5], v[52:53], v[6:7] op_sel:[1,0,0]
	v_pk_add_f32 v[30:31], v[34:35], v[76:77]
	v_pk_fma_f32 v[6:7], v[36:37], v[62:63], v[6:7] op_sel_hi:[0,1,1]
	v_pk_fma_f32 v[8:9], v[36:37], v[70:71], v[6:7] op_sel:[1,0,0]
	v_pk_fma_f32 v[6:7], v[4:5], v[58:59], v[32:33] op_sel_hi:[0,1,1]
	v_pk_fma_f32 v[4:5], v[4:5], v[54:55], v[6:7] op_sel:[1,0,0]
	v_mul_f32_e32 v38, v36, v74
	v_pk_fma_f32 v[4:5], v[36:37], v[72:73], v[4:5] op_sel_hi:[0,1,1]
	v_pk_add_f32 v[30:31], v[30:31], v[56:57]
	v_mov_b32_e32 v39, v46
	v_pk_fma_f32 v[6:7], v[36:37], v[64:65], v[4:5] op_sel:[1,0,0]
	v_mul_f32_e32 v4, v37, v66
	v_pk_add_f32 v[30:31], v[30:31], v[38:39]
	v_mov_b32_e32 v5, v47
	v_pk_add_f32 v[4:5], v[30:31], v[4:5]
	v_lshl_add_u64 v[30:31], v[28:29], 0, v[16:17]
	v_add_co_u32_e32 v76, vcc, 0x200000, v30
	v_lshl_add_u64 v[34:35], s[6:7], 0, v[16:17]
	s_nop 0
	v_addc_co_u32_e32 v77, vcc, 0, v31, vcc
	v_add_co_u32_e32 v78, vcc, s79, v34
	v_mov_b64_e32 v[30:31], v[112:113]
	v_mov_b64_e32 v[32:33], v[114:115]
	s_nop 0
	v_addc_co_u32_e32 v79, vcc, 0, v35, vcc
	v_mov_b64_e32 v[34:35], v[144:145]
	v_mov_b64_e32 v[36:37], v[146:147]
	v_lshl_add_u64 v[38:39], v[14:15], 0, s[8:9]
	s_waitcnt vmcnt(15)
	v_mov_b64_e32 v[46:47], v[152:153]
	v_mov_b64_e32 v[48:49], v[154:155]
	s_waitcnt vmcnt(14)
	v_mov_b64_e32 v[50:51], v[156:157]
	v_mov_b64_e32 v[52:53], v[158:159]
	s_waitcnt vmcnt(13)
	v_mov_b64_e32 v[54:55], v[160:161]
	v_mov_b64_e32 v[56:57], v[162:163]
	s_waitcnt vmcnt(12)
	v_mov_b64_e32 v[58:59], v[164:165]
	v_mov_b64_e32 v[60:61], v[166:167]
	s_mov_b64 s[0:1], 0x2000
	s_add_u32 s8, s8, 0x4000
	s_addc_u32 s9, s9, 0
	s_add_u32 s6, s6, 0x800
	s_addc_u32 s7, s7, 0
	v_lshl_add_u64 v[28:29], v[28:29], 0, s[56:57]
	s_cmp_lg_u32 s8, 0x10000
	v_pk_mul_f32 v[30:31], v[26:27], v[30:31]
	v_pk_mul_f32 v[34:35], v[30:31], v[34:35]
	v_mov_b32_e32 v31, v57
	v_mul_f32_e32 v80, v34, v60
	v_mov_b32_e32 v30, v61
	s_waitcnt vmcnt(11)
	v_mov_b64_e32 v[60:61], v[168:169]
	v_mov_b64_e32 v[62:63], v[170:171]
	s_waitcnt vmcnt(10)
	v_mov_b64_e32 v[64:65], v[172:173]
	v_mov_b64_e32 v[66:67], v[174:175]
	s_waitcnt vmcnt(9)
	v_mov_b64_e32 v[68:69], v[176:177]
	v_mov_b64_e32 v[70:71], v[178:179]
	s_waitcnt vmcnt(8)
	v_mov_b64_e32 v[72:73], v[184:185]
	v_mov_b64_e32 v[74:75], v[186:187]
	v_pk_mul_f32 v[82:83], v[34:35], v[30:31]
	v_pk_fma_f32 v[10:11], v[34:35], v[50:51], v[10:11] op_sel_hi:[0,1,1]
	v_pk_mul_f32 v[30:31], v[26:27], v[32:33]
	v_pk_fma_f32 v[6:7], v[34:35], v[58:59], v[6:7] op_sel_hi:[0,1,1]
	v_pk_fma_f32 v[10:11], v[34:35], v[46:47], v[10:11] op_sel:[1,0,0]
	v_pk_mul_f32 v[46:47], v[30:31], v[36:37]
	v_pk_fma_f32 v[6:7], v[34:35], v[54:55], v[6:7] op_sel:[1,0,0]
	v_mov_b32_e32 v81, v82
	v_mul_f32_e32 v56, v35, v56
	v_pk_fma_f32 v[8:9], v[34:35], v[52:53], v[8:9] op_sel_hi:[0,1,1]
	v_pk_add_f32 v[4:5], v[4:5], v[80:81]
	v_mov_b32_e32 v57, v83
	v_pk_fma_f32 v[8:9], v[34:35], v[48:49], v[8:9] op_sel:[1,0,0]
	v_pk_add_f32 v[4:5], v[4:5], v[56:57]
	v_lshl_add_u64 v[58:59], v[38:39], 0, s[0:1]
	s_mov_b64 s[0:1], 0x2040
	v_mov_b32_e32 v31, v63
	v_pk_fma_f32 v[10:11], v[46:47], v[68:69], v[10:11] op_sel_hi:[0,1,1]
	v_mov_b32_e32 v30, v75
	v_mul_f32_e32 v50, v46, v74
	v_pk_mul_f32 v[74:75], v[46:47], v[30:31]
	v_pk_fma_f32 v[6:7], v[46:47], v[72:73], v[6:7] op_sel_hi:[0,1,1]
	v_pk_fma_f32 v[32:33], v[46:47], v[60:61], v[6:7] op_sel:[1,0,0]
	v_mul_f32_e32 v6, v47, v62
	v_mov_b32_e32 v51, v74
	v_add_co_u32_e32 v62, vcc, s79, v38
	v_pk_fma_f32 v[8:9], v[46:47], v[70:71], v[8:9] op_sel_hi:[0,1,1]
	v_pk_add_f32 v[4:5], v[4:5], v[50:51]
	v_mov_b32_e32 v7, v75
	v_addc_co_u32_e32 v63, vcc, 0, v39, vcc
	v_pk_fma_f32 v[36:37], v[46:47], v[64:65], v[10:11] op_sel:[1,0,0]
	v_pk_fma_f32 v[30:31], v[46:47], v[66:67], v[8:9] op_sel:[1,0,0]
	v_pk_add_f32 v[34:35], v[4:5], v[6:7]
	v_mov_b64_e32 v[4:5], v[116:117]
	v_mov_b64_e32 v[6:7], v[118:119]
	v_mov_b64_e32 v[8:9], v[148:149]
	v_mov_b64_e32 v[10:11], v[150:151]
	s_waitcnt vmcnt(7)
	v_mov_b64_e32 v[46:47], v[188:189]
	v_mov_b64_e32 v[48:49], v[190:191]
	s_waitcnt vmcnt(6)
	v_mov_b64_e32 v[50:51], v[192:193]
	v_mov_b64_e32 v[52:53], v[194:195]
	s_waitcnt vmcnt(5)
	v_mov_b64_e32 v[54:55], v[196:197]
	v_mov_b64_e32 v[56:57], v[198:199]
	s_nop 0
	s_waitcnt vmcnt(4)
	v_mov_b64_e32 v[58:59], v[200:201]
	v_mov_b64_e32 v[60:61], v[202:203]
	v_pk_mul_f32 v[4:5], v[26:27], v[4:5]
	v_pk_mul_f32 v[4:5], v[4:5], v[8:9]
	v_mov_b32_e32 v8, v61
	v_mov_b32_e32 v9, v57
	v_mul_f32_e32 v76, v4, v60
	v_pk_mul_f32 v[78:79], v[4:5], v[8:9]
	v_lshl_add_u64 v[8:9], v[38:39], 0, s[0:1]
	s_waitcnt vmcnt(3)
	v_mov_b64_e32 v[60:61], v[204:205]
	v_mov_b64_e32 v[62:63], v[206:207]
	s_nop 0
	s_waitcnt vmcnt(2)
	v_mov_b64_e32 v[64:65], v[208:209]
	v_mov_b64_e32 v[66:67], v[210:211]
	s_waitcnt vmcnt(1)
	v_mov_b64_e32 v[68:69], v[216:217]
	v_mov_b64_e32 v[70:71], v[218:219]
	s_waitcnt vmcnt(0)
	v_mov_b64_e32 v[72:73], v[220:221]
	v_mov_b64_e32 v[74:75], v[222:223]
	v_pk_fma_f32 v[8:9], v[4:5], v[46:47], v[36:37] op_sel_hi:[0,1,1]
	v_pk_mul_f32 v[6:7], v[26:27], v[6:7]
	v_pk_fma_f32 v[8:9], v[4:5], v[50:51], v[8:9] op_sel:[1,0,0]
	v_pk_mul_f32 v[36:37], v[6:7], v[10:11]
	v_mov_b32_e32 v77, v78
	v_mul_f32_e32 v56, v5, v56
	v_mov_b32_e32 v57, v79
	v_mov_b32_e32 v7, v67
	v_mov_b32_e32 v6, v75
	v_pk_mul_f32 v[46:47], v[36:37], v[6:7]
	v_pk_fma_f32 v[6:7], v[36:37], v[60:61], v[8:9] op_sel_hi:[0,1,1]
	v_pk_fma_f32 v[10:11], v[36:37], v[68:69], v[6:7] op_sel:[1,0,0]
	v_pk_fma_f32 v[6:7], v[4:5], v[48:49], v[30:31] op_sel_hi:[0,1,1]
	v_pk_fma_f32 v[6:7], v[4:5], v[52:53], v[6:7] op_sel:[1,0,0]
	v_pk_add_f32 v[30:31], v[34:35], v[76:77]
	v_pk_fma_f32 v[6:7], v[36:37], v[62:63], v[6:7] op_sel_hi:[0,1,1]
	v_pk_fma_f32 v[8:9], v[36:37], v[70:71], v[6:7] op_sel:[1,0,0]
	v_pk_fma_f32 v[6:7], v[4:5], v[58:59], v[32:33] op_sel_hi:[0,1,1]
	v_pk_fma_f32 v[4:5], v[4:5], v[54:55], v[6:7] op_sel:[1,0,0]
	v_mul_f32_e32 v38, v36, v74
	v_pk_fma_f32 v[4:5], v[36:37], v[72:73], v[4:5] op_sel_hi:[0,1,1]
	v_pk_add_f32 v[30:31], v[30:31], v[56:57]
	v_mov_b32_e32 v39, v46
	v_pk_fma_f32 v[6:7], v[36:37], v[64:65], v[4:5] op_sel:[1,0,0]
	v_mul_f32_e32 v4, v37, v66
	v_pk_add_f32 v[30:31], v[30:31], v[38:39]
	v_mov_b32_e32 v5, v47
	v_pk_add_f32 v[4:5], v[30:31], v[4:5]
	ds_bpermute_b32 v27, v25, v8
	ds_bpermute_b32 v28, v25, v10
	ds_bpermute_b32 v29, v25, v11
	s_mov_b32 s0, 0xff800000
	s_waitcnt lgkmcnt(2)
	v_add_f32_e32 v8, v8, v27
	ds_bpermute_b32 v27, v40, v8
	s_waitcnt lgkmcnt(1)
	v_pk_add_f32 v[10:11], v[10:11], v[28:29]
	ds_bpermute_b32 v28, v40, v10
	ds_bpermute_b32 v29, v40, v11
	s_waitcnt lgkmcnt(2)
	v_add_f32_e32 v8, v8, v27
	ds_bpermute_b32 v27, v41, v8
	s_waitcnt lgkmcnt(1)
	v_pk_add_f32 v[10:11], v[10:11], v[28:29]
	ds_bpermute_b32 v28, v41, v10
	ds_bpermute_b32 v29, v41, v11
	s_waitcnt lgkmcnt(2)
	v_add_f32_e32 v8, v8, v27
	ds_bpermute_b32 v27, v42, v8
	s_waitcnt lgkmcnt(1)
	v_pk_add_f32 v[10:11], v[10:11], v[28:29]
	ds_bpermute_b32 v28, v42, v10
	s_waitcnt lgkmcnt(1)
	v_add_f32_e32 v8, v8, v27
	ds_bpermute_b32 v27, v43, v8
	ds_bpermute_b32 v29, v42, v11
	s_waitcnt lgkmcnt(1)
	v_add_f32_e32 v8, v8, v27
	ds_bpermute_b32 v27, v44, v8
	s_waitcnt lgkmcnt(1)
	v_pk_add_f32 v[10:11], v[10:11], v[28:29]
	ds_bpermute_b32 v28, v43, v10
	ds_bpermute_b32 v29, v43, v11
	s_waitcnt lgkmcnt(2)
	v_add_f32_e32 v8, v8, v27
	ds_bpermute_b32 v27, v25, v9
	s_waitcnt lgkmcnt(1)
	v_pk_add_f32 v[10:11], v[10:11], v[28:29]
	ds_bpermute_b32 v28, v44, v10
	ds_bpermute_b32 v29, v44, v11
	s_waitcnt lgkmcnt(2)
	v_add_f32_e32 v9, v9, v27
	ds_bpermute_b32 v27, v40, v9
	s_waitcnt lgkmcnt(1)
	v_pk_add_f32 v[10:11], v[10:11], v[28:29]
	s_nop 0
	v_cmp_gt_f32_e32 vcc, v11, v10
	s_waitcnt lgkmcnt(0)
	v_add_f32_e32 v9, v9, v27
	ds_bpermute_b32 v27, v41, v9
	v_cmp_nlg_f32_e64 s[10:11], s0, v10
	s_waitcnt lgkmcnt(0)
	v_add_f32_e32 v9, v9, v27
	ds_bpermute_b32 v27, v42, v9
	s_waitcnt lgkmcnt(0)
	v_add_f32_e32 v9, v9, v27
	ds_bpermute_b32 v27, v43, v9
	s_waitcnt lgkmcnt(0)
	v_add_f32_e32 v9, v9, v27
	ds_bpermute_b32 v27, v44, v9
	s_waitcnt lgkmcnt(0)
	v_add_f32_e32 v9, v9, v27
	ds_bpermute_b32 v27, v25, v6
	s_waitcnt lgkmcnt(0)
	v_add_f32_e32 v6, v6, v27
	ds_bpermute_b32 v27, v40, v6
	s_waitcnt lgkmcnt(0)
	v_add_f32_e32 v6, v6, v27
	ds_bpermute_b32 v27, v41, v6
	s_waitcnt lgkmcnt(0)
	v_add_f32_e32 v6, v6, v27
	ds_bpermute_b32 v27, v42, v6
	s_waitcnt lgkmcnt(0)
	v_add_f32_e32 v6, v6, v27
	ds_bpermute_b32 v27, v43, v6
	s_waitcnt lgkmcnt(0)
	v_add_f32_e32 v6, v6, v27
	ds_bpermute_b32 v27, v44, v6
	s_waitcnt lgkmcnt(0)
	v_add_f32_e32 v27, v6, v27
	ds_bpermute_b32 v6, v25, v7
	s_waitcnt lgkmcnt(0)
	v_add_f32_e32 v6, v7, v6
	ds_bpermute_b32 v7, v40, v6
	s_waitcnt lgkmcnt(0)
	v_add_f32_e32 v6, v6, v7
	ds_bpermute_b32 v7, v41, v6
	s_waitcnt lgkmcnt(0)
	v_add_f32_e32 v6, v6, v7
	ds_bpermute_b32 v7, v42, v6
	s_waitcnt lgkmcnt(0)
	v_add_f32_e32 v6, v6, v7
	ds_bpermute_b32 v7, v43, v6
	s_waitcnt lgkmcnt(0)
	v_add_f32_e32 v6, v6, v7
	ds_bpermute_b32 v7, v44, v6
	s_waitcnt lgkmcnt(0)
	v_add_f32_e32 v28, v6, v7
	ds_bpermute_b32 v6, v25, v4
	s_waitcnt lgkmcnt(0)
	v_add_f32_e32 v4, v4, v6
	ds_bpermute_b32 v6, v40, v4
	s_waitcnt lgkmcnt(0)
	v_add_f32_e32 v4, v4, v6
	ds_bpermute_b32 v6, v41, v4
	s_waitcnt lgkmcnt(0)
	v_add_f32_e32 v4, v4, v6
	ds_bpermute_b32 v6, v42, v4
	s_waitcnt lgkmcnt(0)
	v_add_f32_e32 v4, v4, v6
	ds_bpermute_b32 v6, v43, v4
	s_waitcnt lgkmcnt(0)
	v_add_f32_e32 v4, v4, v6
	ds_bpermute_b32 v6, v44, v4
	s_waitcnt lgkmcnt(0)
	v_add_f32_e32 v29, v4, v6
	ds_bpermute_b32 v4, v25, v5
	s_waitcnt lgkmcnt(0)
	v_add_f32_e32 v4, v5, v4
	ds_bpermute_b32 v5, v40, v4
	s_waitcnt lgkmcnt(0)
	v_add_f32_e32 v4, v4, v5
	ds_bpermute_b32 v5, v41, v4
	s_waitcnt lgkmcnt(0)
	v_add_f32_e32 v4, v4, v5
	ds_bpermute_b32 v5, v42, v4
	s_waitcnt lgkmcnt(0)
	v_add_f32_e32 v4, v4, v5
	ds_bpermute_b32 v5, v43, v4
	s_waitcnt lgkmcnt(0)
	v_add_f32_e32 v4, v4, v5
	ds_bpermute_b32 v5, v44, v4
	s_waitcnt lgkmcnt(0)
	v_add_f32_e32 v6, v4, v5
	v_cndmask_b32_e32 v5, v10, v11, vcc
	v_cndmask_b32_e64 v4, 0, 1, vcc
	v_cmp_gt_f32_e32 vcc, v8, v5
	s_nop 1
	v_cndmask_b32_e32 v5, v5, v8, vcc
	v_cndmask_b32_e64 v4, v4, 2, vcc
	v_cmp_gt_f32_e32 vcc, v9, v5
	s_nop 1
	v_cndmask_b32_e32 v5, v5, v9, vcc
	v_cndmask_b32_e64 v4, v4, 3, vcc
	v_cmp_gt_f32_e32 vcc, v27, v5
	s_nop 1
	v_cndmask_b32_e32 v5, v5, v27, vcc
	v_cndmask_b32_e64 v4, v4, 4, vcc
	v_cmp_gt_f32_e32 vcc, v28, v5
	s_nop 1
	v_cndmask_b32_e32 v5, v5, v28, vcc
	v_cmp_gt_f32_e64 s[6:7], v29, v5
	v_cndmask_b32_e64 v4, v4, 5, vcc
	s_nop 0
	v_cndmask_b32_e64 v7, v5, v29, s[6:7]
	v_cndmask_b32_e64 v4, v4, 6, s[6:7]
	v_cmp_ngt_f32_e32 vcc, v6, v7
	s_and_b64 s[0:1], s[6:7], vcc
	s_nop 0
	v_cndmask_b32_e32 v4, 7, v4, vcc
	v_cmp_eq_u32_e64 s[8:9], 0, v4
	s_or_b64 s[8:9], s[8:9], s[10:11]
	s_nop 0
	v_cndmask_b32_e64 v10, v10, v226, s[8:9]
	v_cndmask_b32_e64 v5, 0, -1, s[8:9]
	v_cmp_ne_u32_e64 s[8:9], 1, v4
	v_cmp_gt_f32_e64 s[10:11], v11, v10
	s_and_b64 s[8:9], s[8:9], s[10:11]
	v_cndmask_b32_e64 v10, v10, v11, s[8:9]
	v_cndmask_b32_e64 v5, v5, 1, s[8:9]
	v_cmp_ne_u32_e64 s[8:9], 2, v4
	v_cmp_gt_f32_e64 s[10:11], v8, v10
	s_and_b64 s[8:9], s[8:9], s[10:11]
	v_cndmask_b32_e64 v8, v10, v8, s[8:9]
	v_cndmask_b32_e64 v5, v5, 2, s[8:9]
	v_cmp_ne_u32_e64 s[8:9], 3, v4
	v_cmp_gt_f32_e64 s[10:11], v9, v8
	s_and_b64 s[8:9], s[8:9], s[10:11]
	v_cndmask_b32_e64 v8, v8, v9, s[8:9]
	v_cndmask_b32_e64 v5, v5, 3, s[8:9]
	v_cmp_ne_u32_e64 s[8:9], 4, v4
	v_cmp_gt_f32_e64 s[10:11], v27, v8
	s_and_b64 s[8:9], s[8:9], s[10:11]
	v_cndmask_b32_e64 v8, v8, v27, s[8:9]
	v_cndmask_b32_e64 v5, v5, 4, s[8:9]
	v_cmp_ne_u32_e64 s[8:9], 5, v4
	v_cmp_gt_f32_e64 s[10:11], v28, v8
	s_and_b64 s[8:9], s[8:9], s[10:11]
	v_cndmask_b32_e64 v8, v8, v28, s[8:9]
	v_cmp_ngt_f32_e64 s[6:7], v29, v8
	s_or_b64 s[6:7], s[0:1], s[6:7]
	v_cndmask_b32_e64 v5, v5, 5, s[8:9]
	v_cndmask_b32_e64 v11, v29, v8, s[6:7]
	v_cndmask_b32_e64 v5, 6, v5, s[6:7]
	v_cmp_gt_f32_e64 s[6:7], v6, v11
	s_and_b64 s[6:7], vcc, s[6:7]
	s_nop 0
	v_cndmask_b32_e64 v8, v5, 7, s[6:7]
	v_ashrrev_i32_e32 v9, 31, v8
	s_and_saveexec_b64 s[0:1], s[4:5]
	s_xor_b64 s[8:9], exec, s[0:1]
	s_or_saveexec_b64 s[8:9], s[8:9]
	v_mov_b32_e32 v5, 0
	v_mov_b32_e32 v10, 0
	s_xor_b64 exec, exec, s[8:9]
	s_cbranch_execz .LBB6_1835
	v_cndmask_b32_e64 v5, v11, v6, s[6:7]
	v_cndmask_b32_e32 v6, v6, v7, vcc
	v_sub_f32_e32 v5, v5, v6
	v_mul_f32_e32 v5, 0x3fb8aa3b, v5
	v_exp_f32_e32 v5, v5
	v_mov_b32_e32 v215, 1
	v_add_f32_e32 v6, 1.0, v5
	v_div_scale_f32 v7, s[0:1], v6, v6, 1.0
	v_rcp_f32_e32 v10, v7
	v_readlane_b32 s0, v254, 16
	v_readlane_b32 s1, v254, 17
	v_fma_f32 v11, -v7, v10, 1.0
	v_fmac_f32_e32 v10, v11, v10
	v_div_scale_f32 v11, vcc, 1.0, v6, 1.0
	v_mul_f32_e32 v27, v11, v10
	v_fma_f32 v28, -v7, v27, v11
	v_fmac_f32_e32 v27, v28, v10
	v_fma_f32 v7, -v7, v27, v11
	v_div_fmas_f32 v7, v7, v10, v27
	v_div_fixup_f32 v6, v7, v6, 1.0
	v_mul_f32_e32 v11, v5, v6
	v_mov_b32_e32 v5, v3
	v_lshl_add_u64 v[28:29], v[4:5], 2, s[0:1]
	v_mov_b32_e32 v7, 1
	global_atomic_add v5, v[28:29], v7, off sc0
	v_lshl_add_u64 v[28:29], v[8:9], 2, s[0:1]
	global_atomic_add v10, v[28:29], v7, off sc0
	v_readlane_b32 s0, v254, 18
	v_lshlrev_b64 v[28:29], 5, v[12:13]
	v_readlane_b32 s1, v254, 19
	v_mov_b32_e32 v7, v8
	s_nop 0
	v_lshl_add_u64 v[28:29], s[0:1], 0, v[28:29]
	s_waitcnt vmcnt(1)
	global_store_dwordx4 v[28:29], v[4:7], off
	s_waitcnt vmcnt(1)
	global_store_dwordx2 v[28:29], v[10:11], off offset:16
